# attention fast path: v_dot2_f32_f16 dots, one token per lane softmax, Vt mapping with 4 consecutive d per lane so outputs store directly as full rows (no LDS transpose), fallback decision barrier at t
# speedup vs baseline: 1.1622x; 1.0197x over previous
_Z8attn_fwdPKDF16_S0_S0_PKjPf:
	s_mov_b64 s[36:37], s[0:1]
	s_mov_b32 s38, s2
	s_load_dwordx4 s[8:11], s[0:1], 0x0
	s_load_dwordx4 s[12:15], s[0:1], 0x10
	s_load_dwordx2 s[16:17], s[0:1], 0x20
	s_lshl_b32 s3, s2, 1
	s_mul_hi_u32 s4, s2, 0xaaaaaaab
	s_and_b32 s3, s3, 14
	s_lshr_b32 s4, s4, 6
	s_add_i32 s6, s3, s4
	s_lshr_b32 s5, s2, 3
	s_mul_hi_u32 s7, s5, 0x15555556
	s_mul_i32 s7, s7, 12
	s_sub_i32 s20, s5, s7
	v_and_b32_e32 v1, 63, v0
	v_readfirstlane_b32 s19, v0
	v_and_b32_e32 v2, 3, v1
	v_lshrrev_b32_e32 v3, 2, v1
	s_lshr_b32 s19, s19, 6
	s_lshl_b32 s18, s19, 5
	s_lshl_b32 s26, s19, 12
	v_lshl_add_u32 v4, v1, 4, s26
	v_mul_u32_u24_e32 v5, 0x6000, v3
	v_lshl_add_u32 v5, v2, 4, v5
	v_add_u32_e32 v6, 0x1800, v5
	v_add_u32_e32 v7, 0x3000, v5
	v_add_u32_e32 v8, 0x4800, v5
	v_min_u32_e32 v9, 47, v1
	v_lshlrev_b32_e32 v9, 2, v9
	s_mul_i32 s21, s6, 0xc00
	s_cmp_lt_u32 s20, 11
	s_cselect_b32 s22, 1, 0
	s_cselect_b32 s40, 0, 0xf149f2ca
	s_add_i32 s22, s20, s22
	s_cmp_gt_u32 s20, 0
	s_cselect_b32 s23, 1, 0
	s_cselect_b32 s41, 0, 0xf149f2ca
	s_sub_i32 s23, s20, s23
	s_cmp_lt_u32 s20, 10
	s_cselect_b32 s24, 2, 0
	s_cselect_b32 s42, 0, 0xf149f2ca
	s_add_i32 s24, s20, s24
	s_cmp_gt_u32 s20, 1
	s_cselect_b32 s25, 2, 0
	s_cselect_b32 s43, 0, 0xf149f2ca
	s_sub_i32 s25, s20, s25
	s_waitcnt lgkmcnt(0)
	s_lshl_b32 s26, s20, 8
	s_add_i32 s26, s26, s21
	s_lshl_b32 s26, s26, 7
	s_add_u32 s44, s10, s26
	s_addc_u32 s45, s11, 0
	s_add_u32 s54, s8, s26
	s_addc_u32 s55, s9, 0
	s_lshl_b32 s27, s20, 8
	s_add_i32 s27, s27, s21
	s_add_i32 s27, s27, s18
	s_lshl_b32 s27, s27, 8
	s_add_u32 s62, s16, s27
	s_addc_u32 s63, s17, 0
	s_lshl_b32 s26, s22, 8
	s_add_i32 s26, s26, s21
	s_lshl_b32 s26, s26, 7
	s_add_u32 s46, s10, s26
	s_addc_u32 s47, s11, 0
	s_lshl_b32 s26, s23, 8
	s_add_i32 s26, s26, s21
	s_lshl_b32 s26, s26, 7
	s_add_u32 s48, s10, s26
	s_addc_u32 s49, s11, 0
	s_lshl_b32 s26, s24, 8
	s_add_i32 s26, s26, s21
	s_lshl_b32 s26, s26, 7
	s_add_u32 s50, s10, s26
	s_addc_u32 s51, s11, 0
	s_lshl_b32 s26, s25, 8
	s_add_i32 s26, s26, s21
	s_lshl_b32 s26, s26, 7
	s_add_u32 s52, s10, s26
	s_addc_u32 s53, s11, 0
	s_mul_i32 s28, s6, 0x30000
	s_add_i32 s28, s28, s18
	s_lshl_b32 s26, s20, 8
	s_add_i32 s26, s26, s28
	s_lshl_b32 s26, s26, 1
	s_add_u32 s56, s12, s26
	s_addc_u32 s57, s13, 0
	s_lshl_b32 s26, s22, 8
	s_add_i32 s26, s26, s28
	s_lshl_b32 s26, s26, 1
	s_add_u32 s58, s12, s26
	s_addc_u32 s59, s13, 0
	s_lshl_b32 s26, s23, 8
	s_add_i32 s26, s26, s28
	s_lshl_b32 s26, s26, 1
	s_add_u32 s60, s12, s26
	s_addc_u32 s61, s13, 0
	s_mul_i32 s26, s6, 0xc0
	s_add_u32 s64, s14, s26
	s_addc_u32 s65, s15, 0
	global_load_dword v10, v9, s[64:65]
	global_load_dwordx4 v[96:99], v4, s[54:55] nt
	global_load_dwordx4 v[100:103], v4, s[54:55] offset:1024 nt
	global_load_dwordx4 v[104:107], v4, s[54:55] offset:2048 nt
	global_load_dwordx4 v[108:111], v4, s[54:55] offset:3072 nt
	global_load_dwordx4 v[112:115], v4, s[44:45]
	global_load_dwordx4 v[116:119], v4, s[44:45] offset:1024
	global_load_dwordx4 v[120:123], v4, s[44:45] offset:2048
	global_load_dwordx4 v[124:127], v4, s[44:45] offset:3072
	global_load_dwordx4 v[128:131], v4, s[46:47]
	global_load_dwordx4 v[132:135], v4, s[46:47] offset:1024
	global_load_dwordx4 v[136:139], v4, s[46:47] offset:2048
	global_load_dwordx4 v[140:143], v4, s[46:47] offset:3072
	global_load_dwordx4 v[144:147], v4, s[48:49]
	global_load_dwordx4 v[148:151], v4, s[48:49] offset:1024
	global_load_dwordx4 v[152:155], v4, s[48:49] offset:2048
	global_load_dwordx4 v[156:159], v4, s[48:49] offset:3072
	global_load_dwordx4 v[160:163], v4, s[50:51]
	global_load_dwordx4 v[164:167], v4, s[50:51] offset:1024
	global_load_dwordx4 v[168:171], v4, s[50:51] offset:2048
	global_load_dwordx4 v[172:175], v4, s[50:51] offset:3072
	global_load_dwordx4 v[176:179], v4, s[52:53]
	global_load_dwordx4 v[180:183], v4, s[52:53] offset:1024
	global_load_dwordx4 v[184:187], v4, s[52:53] offset:2048
	global_load_dwordx4 v[188:191], v4, s[52:53] offset:3072
	global_load_dwordx4 v[192:195], v5, s[56:57]
	global_load_dwordx4 v[196:199], v6, s[56:57]
	global_load_dwordx4 v[200:203], v7, s[56:57]
	global_load_dwordx4 v[204:207], v8, s[56:57]
	global_load_dwordx4 v[208:211], v5, s[58:59]
	global_load_dwordx4 v[212:215], v6, s[58:59]
	global_load_dwordx4 v[216:219], v7, s[58:59]
	global_load_dwordx4 v[220:223], v8, s[58:59]
	global_load_dwordx4 v[224:227], v5, s[60:61]
	global_load_dwordx4 v[228:231], v6, s[60:61]
	global_load_dwordx4 v[232:235], v7, s[60:61]
	global_load_dwordx4 v[236:239], v8, s[60:61]
	s_waitcnt vmcnt(32)
	v_max_f32_dpp v11, v10, v10 quad_perm:[1,0,3,2] row_mask:0xf bank_mask:0xf
	v_dot2_f32_f16 v64, v96, v96, 0
	v_dot2_f32_f16 v65, v100, v100, 0
	v_dot2_f32_f16 v66, v104, v104, 0
	v_dot2_f32_f16 v67, v108, v108, 0
	v_max_f32_dpp v11, v11, v11 quad_perm:[2,3,0,1] row_mask:0xf bank_mask:0xf
	v_dot2_f32_f16 v64, v97, v97, v64
	v_dot2_f32_f16 v65, v101, v101, v65
	v_dot2_f32_f16 v66, v105, v105, v66
	v_dot2_f32_f16 v67, v109, v109, v67
	v_max_f32_dpp v11, v11, v11 row_half_mirror row_mask:0xf bank_mask:0xf
	v_dot2_f32_f16 v64, v98, v98, v64
	v_dot2_f32_f16 v65, v102, v102, v65
	v_dot2_f32_f16 v66, v106, v106, v66
	v_dot2_f32_f16 v67, v110, v110, v67
	v_max_f32_dpp v11, v11, v11 row_mirror row_mask:0xf bank_mask:0xf
	v_dot2_f32_f16 v64, v99, v99, v64
	v_dot2_f32_f16 v65, v103, v103, v65
	v_dot2_f32_f16 v66, v107, v107, v66
	v_dot2_f32_f16 v67, v111, v111, v67
	s_nop 2
	v_add_f32_dpp v64, v64, v64 quad_perm:[1,0,3,2] row_mask:0xf bank_mask:0xf
	v_add_f32_dpp v65, v65, v65 quad_perm:[1,0,3,2] row_mask:0xf bank_mask:0xf
	v_add_f32_dpp v66, v66, v66 quad_perm:[1,0,3,2] row_mask:0xf bank_mask:0xf
	v_add_f32_dpp v67, v67, v67 quad_perm:[1,0,3,2] row_mask:0xf bank_mask:0xf
	v_add_f32_dpp v64, v64, v64 quad_perm:[2,3,0,1] row_mask:0xf bank_mask:0xf
	v_add_f32_dpp v65, v65, v65 quad_perm:[2,3,0,1] row_mask:0xf bank_mask:0xf
	v_add_f32_dpp v66, v66, v66 quad_perm:[2,3,0,1] row_mask:0xf bank_mask:0xf
	v_add_f32_dpp v67, v67, v67 quad_perm:[2,3,0,1] row_mask:0xf bank_mask:0xf
	v_add_f32_dpp v64, v64, v64 row_half_mirror row_mask:0xf bank_mask:0xf
	v_add_f32_dpp v65, v65, v65 row_half_mirror row_mask:0xf bank_mask:0xf
	v_add_f32_dpp v66, v66, v66 row_half_mirror row_mask:0xf bank_mask:0xf
	v_add_f32_dpp v67, v67, v67 row_half_mirror row_mask:0xf bank_mask:0xf
	v_max3_f32 v68, v64, v65, v66
	v_readlane_b32 s26, v11, 0
	v_max_f32_e32 v68, v68, v67
	v_readlane_b32 s27, v11, 16
	v_readlane_b32 s28, v11, 32
	v_max_f32_dpp v68, v68, v68 row_mirror row_mask:0xf bank_mask:0xf
	v_readlane_b32 s29, v11, 48
	v_mov_b32_e32 v69, s26
	v_max_f32_e32 v69, s27, v69
	v_max_f32_e32 v69, s28, v69
	v_max_f32_e32 v69, s29, v69
	v_readlane_b32 s26, v68, 0
	v_readlane_b32 s27, v68, 16
	v_readlane_b32 s28, v68, 32
	v_readlane_b32 s29, v68, 48
	v_sqrt_f32_e32 v69, v69
	v_mov_b32_e32 v70, s26
	v_max_f32_e32 v70, s27, v70
	v_max_f32_e32 v70, s28, v70
	v_max_f32_e32 v70, s29, v70
	v_mul_f32_e32 v69, 0x3f8020c5, v69
	v_sqrt_f32_e32 v70, v70
	s_nop 0
	v_mul_f32_e32 v70, 0x3f8020c5, v70
	v_mul_f32_e32 v69, v69, v70
	v_add_f32_e32 v69, 0x42191384, v69
	s_waitcnt vmcnt(28)
	v_dot2_f32_f16 v12, v96, v112, 0
	v_dot2_f32_f16 v13, v100, v116, 0
	v_dot2_f32_f16 v14, v104, v120, 0
	v_dot2_f32_f16 v15, v108, v124, 0
	v_dot2_f32_f16 v12, v97, v113, v12
	v_dot2_f32_f16 v13, v101, v117, v13
	v_dot2_f32_f16 v14, v105, v121, v14
	v_dot2_f32_f16 v15, v109, v125, v15
	v_dot2_f32_f16 v12, v98, v114, v12
	v_dot2_f32_f16 v13, v102, v118, v13
	v_dot2_f32_f16 v14, v106, v122, v14
	v_dot2_f32_f16 v15, v110, v126, v15
	v_dot2_f32_f16 v12, v99, v115, v12
	v_dot2_f32_f16 v13, v103, v119, v13
	v_dot2_f32_f16 v14, v107, v123, v14
	v_dot2_f32_f16 v15, v111, v127, v15
	s_waitcnt vmcnt(24)
	v_dot2_f32_f16 v16, v96, v128, 0
	v_dot2_f32_f16 v17, v100, v132, 0
	v_dot2_f32_f16 v18, v104, v136, 0
	v_dot2_f32_f16 v19, v108, v140, 0
	v_dot2_f32_f16 v16, v97, v129, v16
	v_dot2_f32_f16 v17, v101, v133, v17
	v_dot2_f32_f16 v18, v105, v137, v18
	v_dot2_f32_f16 v19, v109, v141, v19
	v_dot2_f32_f16 v16, v98, v130, v16
	v_dot2_f32_f16 v17, v102, v134, v17
	v_dot2_f32_f16 v18, v106, v138, v18
	v_dot2_f32_f16 v19, v110, v142, v19
	v_dot2_f32_f16 v16, v99, v131, v16
	v_dot2_f32_f16 v17, v103, v135, v17
	v_dot2_f32_f16 v18, v107, v139, v18
	v_dot2_f32_f16 v19, v111, v143, v19
	s_waitcnt vmcnt(20)
	v_dot2_f32_f16 v20, v96, v144, 0
	v_dot2_f32_f16 v21, v100, v148, 0
	v_dot2_f32_f16 v22, v104, v152, 0
	v_dot2_f32_f16 v23, v108, v156, 0
	v_dot2_f32_f16 v20, v97, v145, v20
	v_dot2_f32_f16 v21, v101, v149, v21
	v_dot2_f32_f16 v22, v105, v153, v22
	v_dot2_f32_f16 v23, v109, v157, v23
	v_dot2_f32_f16 v20, v98, v146, v20
	v_dot2_f32_f16 v21, v102, v150, v21
	v_dot2_f32_f16 v22, v106, v154, v22
	v_dot2_f32_f16 v23, v110, v158, v23
	v_dot2_f32_f16 v20, v99, v147, v20
	v_dot2_f32_f16 v21, v103, v151, v21
	v_dot2_f32_f16 v22, v107, v155, v22
	v_dot2_f32_f16 v23, v111, v159, v23
	s_waitcnt vmcnt(16)
	v_dot2_f32_f16 v24, v96, v160, 0
	v_dot2_f32_f16 v25, v100, v164, 0
	v_dot2_f32_f16 v26, v104, v168, 0
	v_dot2_f32_f16 v27, v108, v172, 0
	v_dot2_f32_f16 v24, v97, v161, v24
	v_dot2_f32_f16 v25, v101, v165, v25
	v_dot2_f32_f16 v26, v105, v169, v26
	v_dot2_f32_f16 v27, v109, v173, v27
	v_dot2_f32_f16 v24, v98, v162, v24
	v_dot2_f32_f16 v25, v102, v166, v25
	v_dot2_f32_f16 v26, v106, v170, v26
	v_dot2_f32_f16 v27, v110, v174, v27
	v_dot2_f32_f16 v24, v99, v163, v24
	v_dot2_f32_f16 v25, v103, v167, v25
	v_dot2_f32_f16 v26, v107, v171, v26
	v_dot2_f32_f16 v27, v111, v175, v27
	s_waitcnt vmcnt(12)
	v_dot2_f32_f16 v28, v96, v176, 0
	v_dot2_f32_f16 v29, v100, v180, 0
	v_dot2_f32_f16 v30, v104, v184, 0
	v_dot2_f32_f16 v31, v108, v188, 0
	v_dot2_f32_f16 v28, v97, v177, v28
	v_dot2_f32_f16 v29, v101, v181, v29
	v_dot2_f32_f16 v30, v105, v185, v30
	v_dot2_f32_f16 v31, v109, v189, v31
	v_dot2_f32_f16 v28, v98, v178, v28
	v_dot2_f32_f16 v29, v102, v182, v29
	v_dot2_f32_f16 v30, v106, v186, v30
	v_dot2_f32_f16 v31, v110, v190, v31
	v_dot2_f32_f16 v28, v99, v179, v28
	v_dot2_f32_f16 v29, v103, v183, v29
	v_dot2_f32_f16 v30, v107, v187, v30
	v_dot2_f32_f16 v31, v111, v191, v31
	s_nop 2
	v_add_f32_dpp v12, v12, v12 quad_perm:[1,0,3,2] row_mask:0xf bank_mask:0xf
	v_add_f32_dpp v13, v13, v13 quad_perm:[1,0,3,2] row_mask:0xf bank_mask:0xf
	v_add_f32_dpp v14, v14, v14 quad_perm:[1,0,3,2] row_mask:0xf bank_mask:0xf
	v_add_f32_dpp v15, v15, v15 quad_perm:[1,0,3,2] row_mask:0xf bank_mask:0xf
	v_add_f32_dpp v16, v16, v16 quad_perm:[1,0,3,2] row_mask:0xf bank_mask:0xf
	v_add_f32_dpp v17, v17, v17 quad_perm:[1,0,3,2] row_mask:0xf bank_mask:0xf
	v_add_f32_dpp v18, v18, v18 quad_perm:[1,0,3,2] row_mask:0xf bank_mask:0xf
	v_add_f32_dpp v19, v19, v19 quad_perm:[1,0,3,2] row_mask:0xf bank_mask:0xf
	v_add_f32_dpp v20, v20, v20 quad_perm:[1,0,3,2] row_mask:0xf bank_mask:0xf
	v_add_f32_dpp v21, v21, v21 quad_perm:[1,0,3,2] row_mask:0xf bank_mask:0xf
	v_add_f32_dpp v22, v22, v22 quad_perm:[1,0,3,2] row_mask:0xf bank_mask:0xf
	v_add_f32_dpp v23, v23, v23 quad_perm:[1,0,3,2] row_mask:0xf bank_mask:0xf
	v_add_f32_dpp v24, v24, v24 quad_perm:[1,0,3,2] row_mask:0xf bank_mask:0xf
	v_add_f32_dpp v25, v25, v25 quad_perm:[1,0,3,2] row_mask:0xf bank_mask:0xf
	v_add_f32_dpp v26, v26, v26 quad_perm:[1,0,3,2] row_mask:0xf bank_mask:0xf
	v_add_f32_dpp v27, v27, v27 quad_perm:[1,0,3,2] row_mask:0xf bank_mask:0xf
	v_add_f32_dpp v28, v28, v28 quad_perm:[1,0,3,2] row_mask:0xf bank_mask:0xf
	v_add_f32_dpp v29, v29, v29 quad_perm:[1,0,3,2] row_mask:0xf bank_mask:0xf
	v_add_f32_dpp v30, v30, v30 quad_perm:[1,0,3,2] row_mask:0xf bank_mask:0xf
	v_add_f32_dpp v31, v31, v31 quad_perm:[1,0,3,2] row_mask:0xf bank_mask:0xf
	v_add_f32_dpp v12, v12, v12 quad_perm:[2,3,0,1] row_mask:0xf bank_mask:0xf
	v_add_f32_dpp v13, v13, v13 quad_perm:[2,3,0,1] row_mask:0xf bank_mask:0xf
	v_add_f32_dpp v14, v14, v14 quad_perm:[2,3,0,1] row_mask:0xf bank_mask:0xf
	v_add_f32_dpp v15, v15, v15 quad_perm:[2,3,0,1] row_mask:0xf bank_mask:0xf
	v_add_f32_dpp v16, v16, v16 quad_perm:[2,3,0,1] row_mask:0xf bank_mask:0xf
	v_add_f32_dpp v17, v17, v17 quad_perm:[2,3,0,1] row_mask:0xf bank_mask:0xf
	v_add_f32_dpp v18, v18, v18 quad_perm:[2,3,0,1] row_mask:0xf bank_mask:0xf
	v_add_f32_dpp v19, v19, v19 quad_perm:[2,3,0,1] row_mask:0xf bank_mask:0xf
	v_add_f32_dpp v20, v20, v20 quad_perm:[2,3,0,1] row_mask:0xf bank_mask:0xf
	v_add_f32_dpp v21, v21, v21 quad_perm:[2,3,0,1] row_mask:0xf bank_mask:0xf
	v_add_f32_dpp v22, v22, v22 quad_perm:[2,3,0,1] row_mask:0xf bank_mask:0xf
	v_add_f32_dpp v23, v23, v23 quad_perm:[2,3,0,1] row_mask:0xf bank_mask:0xf
	v_add_f32_dpp v24, v24, v24 quad_perm:[2,3,0,1] row_mask:0xf bank_mask:0xf
	v_add_f32_dpp v25, v25, v25 quad_perm:[2,3,0,1] row_mask:0xf bank_mask:0xf
	v_add_f32_dpp v26, v26, v26 quad_perm:[2,3,0,1] row_mask:0xf bank_mask:0xf
	v_add_f32_dpp v27, v27, v27 quad_perm:[2,3,0,1] row_mask:0xf bank_mask:0xf
	v_add_f32_dpp v28, v28, v28 quad_perm:[2,3,0,1] row_mask:0xf bank_mask:0xf
	v_add_f32_dpp v29, v29, v29 quad_perm:[2,3,0,1] row_mask:0xf bank_mask:0xf
	v_add_f32_dpp v30, v30, v30 quad_perm:[2,3,0,1] row_mask:0xf bank_mask:0xf
	v_add_f32_dpp v31, v31, v31 quad_perm:[2,3,0,1] row_mask:0xf bank_mask:0xf
	v_add_f32_dpp v12, v12, v12 row_half_mirror row_mask:0xf bank_mask:0xf
	v_add_f32_dpp v13, v13, v13 row_half_mirror row_mask:0xf bank_mask:0xf
	v_add_f32_dpp v14, v14, v14 row_half_mirror row_mask:0xf bank_mask:0xf
	v_add_f32_dpp v15, v15, v15 row_half_mirror row_mask:0xf bank_mask:0xf
	v_add_f32_dpp v16, v16, v16 row_half_mirror row_mask:0xf bank_mask:0xf
	v_add_f32_dpp v17, v17, v17 row_half_mirror row_mask:0xf bank_mask:0xf
	v_add_f32_dpp v18, v18, v18 row_half_mirror row_mask:0xf bank_mask:0xf
	v_add_f32_dpp v19, v19, v19 row_half_mirror row_mask:0xf bank_mask:0xf
	v_add_f32_dpp v20, v20, v20 row_half_mirror row_mask:0xf bank_mask:0xf
	v_add_f32_dpp v21, v21, v21 row_half_mirror row_mask:0xf bank_mask:0xf
	v_add_f32_dpp v22, v22, v22 row_half_mirror row_mask:0xf bank_mask:0xf
	v_add_f32_dpp v23, v23, v23 row_half_mirror row_mask:0xf bank_mask:0xf
	v_add_f32_dpp v24, v24, v24 row_half_mirror row_mask:0xf bank_mask:0xf
	v_add_f32_dpp v25, v25, v25 row_half_mirror row_mask:0xf bank_mask:0xf
	v_add_f32_dpp v26, v26, v26 row_half_mirror row_mask:0xf bank_mask:0xf
	v_add_f32_dpp v27, v27, v27 row_half_mirror row_mask:0xf bank_mask:0xf
	v_add_f32_dpp v28, v28, v28 row_half_mirror row_mask:0xf bank_mask:0xf
	v_add_f32_dpp v29, v29, v29 row_half_mirror row_mask:0xf bank_mask:0xf
	v_add_f32_dpp v30, v30, v30 row_half_mirror row_mask:0xf bank_mask:0xf
	v_add_f32_dpp v31, v31, v31 row_half_mirror row_mask:0xf bank_mask:0xf
	v_cmp_eq_u32_e64 s[70:71], 1, v2
	v_cmp_eq_u32_e64 s[72:73], 2, v2
	v_cmp_eq_u32_e64 s[74:75], 3, v2
	v_cndmask_b32_e64 v112, v12, v13, s[70:71]
	v_cndmask_b32_e64 v113, v16, v17, s[70:71]
	v_cndmask_b32_e64 v114, v20, v21, s[70:71]
	v_cndmask_b32_e64 v115, v24, v25, s[70:71]
	v_cndmask_b32_e64 v116, v28, v29, s[70:71]
	v_cndmask_b32_e64 v112, v112, v14, s[72:73]
	v_cndmask_b32_e64 v113, v113, v18, s[72:73]
	v_cndmask_b32_e64 v114, v114, v22, s[72:73]
	v_cndmask_b32_e64 v115, v115, v26, s[72:73]
	v_cndmask_b32_e64 v116, v116, v30, s[72:73]
	v_cndmask_b32_e64 v112, v112, v15, s[74:75]
	v_cndmask_b32_e64 v113, v113, v19, s[74:75]
	v_cndmask_b32_e64 v114, v114, v23, s[74:75]
	v_cndmask_b32_e64 v115, v115, v27, s[74:75]
	v_cndmask_b32_e64 v116, v116, v31, s[74:75]
	v_add_f32_e32 v112, 0x42e59caf, v112
	v_add_f32_e32 v113, 0x42e59caf, v113
	v_add_f32_e32 v114, 0x42e59caf, v114
	v_add_f32_e32 v115, 0x42659caf, v115
	v_add_f32_e32 v116, 0x42659caf, v116
	v_add_f32_e32 v113, s40, v113
	v_add_f32_e32 v114, s41, v114
	v_add_f32_e32 v115, s42, v115
	v_add_f32_e32 v116, s43, v116
	v_max3_f32 v117, v112, v113, v114
	v_max_f32_e32 v118, v115, v116
	v_sub_f32_e32 v120, v112, v117
	v_sub_f32_e32 v121, v113, v117
	v_sub_f32_e32 v122, v114, v117
	v_sub_f32_e32 v118, v118, v117
	v_exp_f32_e32 v120, v120
	v_exp_f32_e32 v121, v121
	v_exp_f32_e32 v122, v122
	v_min_f32_dpp v119, v117, v117 quad_perm:[1,0,3,2] row_mask:0xf bank_mask:0xf
	s_mov_b32 s30, 0xc2200a3d
	v_cmp_ngt_f32_e32 vcc, s30, v118
	v_min_f32_dpp v119, v119, v119 quad_perm:[2,3,0,1] row_mask:0xf bank_mask:0xf
	s_cmp_lg_u64 vcc, 0
	s_cselect_b32 s31, 1, 0
	v_min_f32_dpp v119, v119, v119 row_half_mirror row_mask:0xf bank_mask:0xf
	v_add_f32_e32 v123, v120, v121
	v_add_f32_e32 v123, v123, v122
	v_min_f32_dpp v119, v119, v119 row_mirror row_mask:0xf bank_mask:0xf
	s_nop 1
	v_readlane_b32 s26, v119, 0
	v_readlane_b32 s27, v119, 16
	v_readlane_b32 s28, v119, 32
	v_readlane_b32 s29, v119, 48
	s_nop 1
	v_mov_b32_e32 v138, s26
	v_min_f32_e32 v138, s27, v138
	v_min_f32_e32 v138, s28, v138
	v_min_f32_e32 v138, s29, v138
	v_sub_f32_e32 v69, v69, v138
	v_cmp_ngt_f32_e32 vcc, s30, v69
	s_cmp_lg_u64 vcc, 0
	s_cselect_b32 s26, 1, 0
	s_or_b32 s31, s31, s26
	s_lshl_b32 s26, s19, 2
	s_add_i32 s26, s26, 0x20700
	v_mov_b32_e32 v139, s26
	v_mov_b32_e32 v140, s31
	ds_write_b32 v139, v140
	v_div_scale_f32 v141, s[26:27], v123, v123, 1.0
	v_rcp_f32_e32 v142, v141
	s_nop 0
	v_fma_f32 v143, -v141, v142, 1.0
	v_fmac_f32_e32 v142, v143, v142
	v_div_scale_f32 v143, vcc, 1.0, v123, 1.0
	v_mul_f32_e32 v144, v143, v142
	v_fma_f32 v145, -v141, v144, v143
	v_fmac_f32_e32 v144, v145, v142
	v_fma_f32 v141, -v141, v144, v143
	v_div_fmas_f32 v141, v141, v142, v144
	v_div_fixup_f32 v123, v141, v123, 1.0
	v_mul_f32_e32 v120, v120, v123
	v_mul_f32_e32 v121, v121, v123
	v_mul_f32_e32 v122, v122, v123
	v_lshrrev_b32_e32 v152, 3, v1
	v_and_b32_e32 v153, 3, v152
	v_lshrrev_b32_e32 v152, 2, v152
	v_lshlrev_b32_e32 v152, 5, v152
	v_lshl_or_b32 v152, v153, 2, v152
	v_and_b32_e32 v153, 1, v2
	v_lshl_or_b32 v152, v153, 4, v152
	v_lshrrev_b32_e32 v153, 1, v2
	v_lshl_or_b32 v152, v153, 6, v152
	s_lshl_b32 s26, s19, 9
	s_add_i32 s26, s26, 0x18000
	v_add_u32_e32 v152, s26, v152
	v_lshl_add_u32 v153, v2, 5, s26
	ds_write_b32 v152, v120
	ds_write_b32 v152, v121 offset:128
	ds_write_b32 v152, v122 offset:256
	ds_read_b128 v[64:67], v153
	ds_read_b128 v[68:71], v153 offset:16
	ds_read_b128 v[72:75], v153 offset:128
	ds_read_b128 v[76:79], v153 offset:144
	ds_read_b128 v[80:83], v153 offset:256
	ds_read_b128 v[84:87], v153 offset:272
	v_lshrrev_b32_e32 v154, 1, v2
	v_and_b32_e32 v155, 1, v2
	v_lshlrev_b32_e32 v154, 4, v154
	v_lshl_or_b32 v154, v155, 2, v154
	v_lshlrev_b32_e32 v154, 8, v154
	v_lshl_add_u32 v154, v3, 4, v154
	s_waitcnt lgkmcnt(0)
	s_waitcnt vmcnt(8)
	v_fma_mix_f32 v32, v192, v64, 0 op_sel:[0,0,0] op_sel_hi:[1,0,0]
	v_fma_mix_f32 v36, v192, v65, 0 op_sel:[1,0,0] op_sel_hi:[1,0,0]
	v_fma_mix_f32 v40, v193, v66, 0 op_sel:[0,0,0] op_sel_hi:[1,0,0]
	v_fma_mix_f32 v44, v193, v67, 0 op_sel:[1,0,0] op_sel_hi:[1,0,0]
	v_fma_mix_f32 v48, v194, v68, 0 op_sel:[0,0,0] op_sel_hi:[1,0,0]
	v_fma_mix_f32 v52, v194, v69, 0 op_sel:[1,0,0] op_sel_hi:[1,0,0]
	v_fma_mix_f32 v56, v195, v70, 0 op_sel:[0,0,0] op_sel_hi:[1,0,0]
	v_fma_mix_f32 v60, v195, v71, 0 op_sel:[1,0,0] op_sel_hi:[1,0,0]
	v_fma_mix_f32 v33, v196, v64, 0 op_sel:[0,0,0] op_sel_hi:[1,0,0]
	v_fma_mix_f32 v37, v196, v65, 0 op_sel:[1,0,0] op_sel_hi:[1,0,0]
	v_fma_mix_f32 v41, v197, v66, 0 op_sel:[0,0,0] op_sel_hi:[1,0,0]
	v_fma_mix_f32 v45, v197, v67, 0 op_sel:[1,0,0] op_sel_hi:[1,0,0]
	v_fma_mix_f32 v49, v198, v68, 0 op_sel:[0,0,0] op_sel_hi:[1,0,0]
	v_fma_mix_f32 v53, v198, v69, 0 op_sel:[1,0,0] op_sel_hi:[1,0,0]
	v_fma_mix_f32 v57, v199, v70, 0 op_sel:[0,0,0] op_sel_hi:[1,0,0]
	v_fma_mix_f32 v61, v199, v71, 0 op_sel:[1,0,0] op_sel_hi:[1,0,0]
	v_fma_mix_f32 v34, v200, v64, 0 op_sel:[0,0,0] op_sel_hi:[1,0,0]
	v_fma_mix_f32 v38, v200, v65, 0 op_sel:[1,0,0] op_sel_hi:[1,0,0]
	v_fma_mix_f32 v42, v201, v66, 0 op_sel:[0,0,0] op_sel_hi:[1,0,0]
	v_fma_mix_f32 v46, v201, v67, 0 op_sel:[1,0,0] op_sel_hi:[1,0,0]
	v_fma_mix_f32 v50, v202, v68, 0 op_sel:[0,0,0] op_sel_hi:[1,0,0]
	v_fma_mix_f32 v54, v202, v69, 0 op_sel:[1,0,0] op_sel_hi:[1,0,0]
	v_fma_mix_f32 v58, v203, v70, 0 op_sel:[0,0,0] op_sel_hi:[1,0,0]
	v_fma_mix_f32 v62, v203, v71, 0 op_sel:[1,0,0] op_sel_hi:[1,0,0]
	v_fma_mix_f32 v35, v204, v64, 0 op_sel:[0,0,0] op_sel_hi:[1,0,0]
	v_fma_mix_f32 v39, v204, v65, 0 op_sel:[1,0,0] op_sel_hi:[1,0,0]
	v_fma_mix_f32 v43, v205, v66, 0 op_sel:[0,0,0] op_sel_hi:[1,0,0]
	v_fma_mix_f32 v47, v205, v67, 0 op_sel:[1,0,0] op_sel_hi:[1,0,0]
	v_fma_mix_f32 v51, v206, v68, 0 op_sel:[0,0,0] op_sel_hi:[1,0,0]
	v_fma_mix_f32 v55, v206, v69, 0 op_sel:[1,0,0] op_sel_hi:[1,0,0]
	v_fma_mix_f32 v59, v207, v70, 0 op_sel:[0,0,0] op_sel_hi:[1,0,0]
	v_fma_mix_f32 v63, v207, v71, 0 op_sel:[1,0,0] op_sel_hi:[1,0,0]
	s_waitcnt vmcnt(4)
	v_fma_mix_f32 v32, v208, v72, v32 op_sel:[0,0,0] op_sel_hi:[1,0,0]
	v_fma_mix_f32 v36, v208, v73, v36 op_sel:[1,0,0] op_sel_hi:[1,0,0]
	v_fma_mix_f32 v40, v209, v74, v40 op_sel:[0,0,0] op_sel_hi:[1,0,0]
	v_fma_mix_f32 v44, v209, v75, v44 op_sel:[1,0,0] op_sel_hi:[1,0,0]
	v_fma_mix_f32 v48, v210, v76, v48 op_sel:[0,0,0] op_sel_hi:[1,0,0]
	v_fma_mix_f32 v52, v210, v77, v52 op_sel:[1,0,0] op_sel_hi:[1,0,0]
	v_fma_mix_f32 v56, v211, v78, v56 op_sel:[0,0,0] op_sel_hi:[1,0,0]
	v_fma_mix_f32 v60, v211, v79, v60 op_sel:[1,0,0] op_sel_hi:[1,0,0]
	v_fma_mix_f32 v33, v212, v72, v33 op_sel:[0,0,0] op_sel_hi:[1,0,0]
	v_fma_mix_f32 v37, v212, v73, v37 op_sel:[1,0,0] op_sel_hi:[1,0,0]
	v_fma_mix_f32 v41, v213, v74, v41 op_sel:[0,0,0] op_sel_hi:[1,0,0]
	v_fma_mix_f32 v45, v213, v75, v45 op_sel:[1,0,0] op_sel_hi:[1,0,0]
	v_fma_mix_f32 v49, v214, v76, v49 op_sel:[0,0,0] op_sel_hi:[1,0,0]
	v_fma_mix_f32 v53, v214, v77, v53 op_sel:[1,0,0] op_sel_hi:[1,0,0]
	v_fma_mix_f32 v57, v215, v78, v57 op_sel:[0,0,0] op_sel_hi:[1,0,0]
	v_fma_mix_f32 v61, v215, v79, v61 op_sel:[1,0,0] op_sel_hi:[1,0,0]
	v_fma_mix_f32 v34, v216, v72, v34 op_sel:[0,0,0] op_sel_hi:[1,0,0]
	v_fma_mix_f32 v38, v216, v73, v38 op_sel:[1,0,0] op_sel_hi:[1,0,0]
	v_fma_mix_f32 v42, v217, v74, v42 op_sel:[0,0,0] op_sel_hi:[1,0,0]
	v_fma_mix_f32 v46, v217, v75, v46 op_sel:[1,0,0] op_sel_hi:[1,0,0]
	v_fma_mix_f32 v50, v218, v76, v50 op_sel:[0,0,0] op_sel_hi:[1,0,0]
	v_fma_mix_f32 v54, v218, v77, v54 op_sel:[1,0,0] op_sel_hi:[1,0,0]
	v_fma_mix_f32 v58, v219, v78, v58 op_sel:[0,0,0] op_sel_hi:[1,0,0]
	v_fma_mix_f32 v62, v219, v79, v62 op_sel:[1,0,0] op_sel_hi:[1,0,0]
	v_fma_mix_f32 v35, v220, v72, v35 op_sel:[0,0,0] op_sel_hi:[1,0,0]
	v_fma_mix_f32 v39, v220, v73, v39 op_sel:[1,0,0] op_sel_hi:[1,0,0]
	v_fma_mix_f32 v43, v221, v74, v43 op_sel:[0,0,0] op_sel_hi:[1,0,0]
	v_fma_mix_f32 v47, v221, v75, v47 op_sel:[1,0,0] op_sel_hi:[1,0,0]
	v_fma_mix_f32 v51, v222, v76, v51 op_sel:[0,0,0] op_sel_hi:[1,0,0]
	v_fma_mix_f32 v55, v222, v77, v55 op_sel:[1,0,0] op_sel_hi:[1,0,0]
	v_fma_mix_f32 v59, v223, v78, v59 op_sel:[0,0,0] op_sel_hi:[1,0,0]
	v_fma_mix_f32 v63, v223, v79, v63 op_sel:[1,0,0] op_sel_hi:[1,0,0]
	s_waitcnt vmcnt(0)
	v_fma_mix_f32 v32, v224, v80, v32 op_sel:[0,0,0] op_sel_hi:[1,0,0]
	v_fma_mix_f32 v36, v224, v81, v36 op_sel:[1,0,0] op_sel_hi:[1,0,0]
	v_fma_mix_f32 v40, v225, v82, v40 op_sel:[0,0,0] op_sel_hi:[1,0,0]
	v_fma_mix_f32 v44, v225, v83, v44 op_sel:[1,0,0] op_sel_hi:[1,0,0]
	v_fma_mix_f32 v48, v226, v84, v48 op_sel:[0,0,0] op_sel_hi:[1,0,0]
	v_fma_mix_f32 v52, v226, v85, v52 op_sel:[1,0,0] op_sel_hi:[1,0,0]
	v_fma_mix_f32 v56, v227, v86, v56 op_sel:[0,0,0] op_sel_hi:[1,0,0]
	v_fma_mix_f32 v60, v227, v87, v60 op_sel:[1,0,0] op_sel_hi:[1,0,0]
	v_fma_mix_f32 v33, v228, v80, v33 op_sel:[0,0,0] op_sel_hi:[1,0,0]
	v_fma_mix_f32 v37, v228, v81, v37 op_sel:[1,0,0] op_sel_hi:[1,0,0]
	v_fma_mix_f32 v41, v229, v82, v41 op_sel:[0,0,0] op_sel_hi:[1,0,0]
	v_fma_mix_f32 v45, v229, v83, v45 op_sel:[1,0,0] op_sel_hi:[1,0,0]
	v_fma_mix_f32 v49, v230, v84, v49 op_sel:[0,0,0] op_sel_hi:[1,0,0]
	v_fma_mix_f32 v53, v230, v85, v53 op_sel:[1,0,0] op_sel_hi:[1,0,0]
	v_fma_mix_f32 v57, v231, v86, v57 op_sel:[0,0,0] op_sel_hi:[1,0,0]
	v_fma_mix_f32 v61, v231, v87, v61 op_sel:[1,0,0] op_sel_hi:[1,0,0]
	v_fma_mix_f32 v34, v232, v80, v34 op_sel:[0,0,0] op_sel_hi:[1,0,0]
	v_fma_mix_f32 v38, v232, v81, v38 op_sel:[1,0,0] op_sel_hi:[1,0,0]
	v_fma_mix_f32 v42, v233, v82, v42 op_sel:[0,0,0] op_sel_hi:[1,0,0]
	v_fma_mix_f32 v46, v233, v83, v46 op_sel:[1,0,0] op_sel_hi:[1,0,0]
	v_fma_mix_f32 v50, v234, v84, v50 op_sel:[0,0,0] op_sel_hi:[1,0,0]
	v_fma_mix_f32 v54, v234, v85, v54 op_sel:[1,0,0] op_sel_hi:[1,0,0]
	v_fma_mix_f32 v58, v235, v86, v58 op_sel:[0,0,0] op_sel_hi:[1,0,0]
	v_fma_mix_f32 v62, v235, v87, v62 op_sel:[1,0,0] op_sel_hi:[1,0,0]
	v_fma_mix_f32 v35, v236, v80, v35 op_sel:[0,0,0] op_sel_hi:[1,0,0]
	v_fma_mix_f32 v39, v236, v81, v39 op_sel:[1,0,0] op_sel_hi:[1,0,0]
	v_fma_mix_f32 v43, v237, v82, v43 op_sel:[0,0,0] op_sel_hi:[1,0,0]
	v_fma_mix_f32 v47, v237, v83, v47 op_sel:[1,0,0] op_sel_hi:[1,0,0]
	v_fma_mix_f32 v51, v238, v84, v51 op_sel:[0,0,0] op_sel_hi:[1,0,0]
	v_fma_mix_f32 v55, v238, v85, v55 op_sel:[1,0,0] op_sel_hi:[1,0,0]
	v_fma_mix_f32 v59, v239, v86, v59 op_sel:[0,0,0] op_sel_hi:[1,0,0]
	v_fma_mix_f32 v63, v239, v87, v63 op_sel:[1,0,0] op_sel_hi:[1,0,0]
	global_store_dwordx4 v154, v[32:35], s[62:63] sc1
	global_store_dwordx4 v154, v[36:39], s[62:63] offset:256 sc1
	global_store_dwordx4 v154, v[40:43], s[62:63] offset:512 sc1
	global_store_dwordx4 v154, v[44:47], s[62:63] offset:768 sc1
	global_store_dwordx4 v154, v[48:51], s[62:63] offset:2048 sc1
	global_store_dwordx4 v154, v[52:55], s[62:63] offset:2304 sc1
	global_store_dwordx4 v154, v[56:59], s[62:63] offset:2560 sc1
	global_store_dwordx4 v154, v[60:63], s[62:63] offset:2816 sc1
	s_waitcnt lgkmcnt(0)
	s_barrier
	v_mov_b32_e32 v139, 0x20700
	ds_read_b128 v[144:147], v139
	ds_read_b128 v[148:151], v139 offset:16
	s_waitcnt lgkmcnt(0)
	v_or3_b32 v144, v144, v145, v146
	v_or3_b32 v148, v148, v149, v150
	v_or3_b32 v144, v144, v147, v148
	v_or_b32_e32 v144, v144, v151
	s_nop 0
	v_readfirstlane_b32 s27, v144
	s_nop 3
	s_cmp_lg_u32 s27, 0
	s_cbranch_scc1 .Lattn_fallback
	s_endpgm
